# baseline (speedup 1.0000x reference)
.Lat_u0:
	ds_read_b128 v[108:111], v193
	ds_read_b128 v[112:115], v193 offset:1024
	v_mfma_i32_32x32x32_i8 v[84:99], v[242:245], v[140:143], v[84:99]
	ds_read_b128 v[116:119], v195 offset:6144
	ds_read_b128 v[120:123], v196 offset:6144
	s_cmp_gt_u32 s43, 29
	s_cbranch_scc1 .Lat_nok0
	s_add_i32 m0, s31, 49152
	ds_read_b128 v[124:127], v195 offset:4096
	global_load_lds_dwordx4 v252, s[60:61]
	s_add_i32 m0, s31, 57344
	v_mfma_i32_32x32x32_i8 v[84:99], v[246:249], v[144:147], v[84:99]
	global_load_lds_dwordx4 v254, s[60:61]

.Lat_u5:
	ds_read_b128 v[108:111], v193 offset:8192
	ds_read_b128 v[112:115], v193 offset:9216
	v_mfma_i32_32x32x32_i8 v[84:99], v[242:245], v[140:143], v[84:99]
	ds_read_b128 v[116:119], v195 offset:38912
	ds_read_b128 v[120:123], v196 offset:38912
	s_cmp_gt_u32 s43, 29
	s_cbranch_scc1 .Lat_nok5
	s_add_i32 m0, s31, 81920
	ds_read_b128 v[124:127], v195 offset:36864
	global_load_lds_dwordx4 v252, s[60:61]
	s_add_i32 m0, s31, 90112
	v_mfma_i32_32x32x32_i8 v[84:99], v[246:249], v[144:147], v[84:99]
	global_load_lds_dwordx4 v254, s[60:61]

.Lat_nok0:
	ds_read_b128 v[124:127], v195 offset:4096
	v_mfma_i32_32x32x32_i8 v[84:99], v[246:249], v[144:147], v[84:99]
	s_branch .Lat_k0
.Lat_nov0:
	v_fma_f32 v84, v84, v250, v251
	v_fma_f32 v85, v85, v250, v251
	s_branch .Lat_v0
.Lat_nok5:
	ds_read_b128 v[124:127], v195 offset:36864
	v_mfma_i32_32x32x32_i8 v[84:99], v[246:249], v[144:147], v[84:99]
	s_branch .Lat_k5
